# prep: A=Wk^T Wq fold blocks load wk/wq with coalesced dwordx4 and transpose through LDS (16 loads/thread instead of 128 dword loads)
# baseline (speedup 1.0000x reference)
.LBB0_34:
	s_andn2_b64 vcc, exec, s[8:9]
	s_cbranch_vccnz .LBB0_38
	v_lshrrev_b32_e32 v1, 2, v0
	s_ashr_i32 s3, s3, 3
	s_lshl_b32 s8, s2, 5
	s_and_b32 s8, s8, 0xe0
	v_lshrrev_b32_e32 v2, 3, v0
	v_and_b32_e32 v3, 7, v0
	v_lshlrev_b32_e32 v4, 13, v2
	v_lshl_or_b32 v4, v3, 4, v4
	v_add_u32_e32 v5, 0x1000, v4
	s_waitcnt lgkmcnt(0)
	s_lshl_b32 s9, s3, 7
	s_add_u32 s10, s6, s9
	s_addc_u32 s11, s7, 0
	s_lshl_b32 s9, s8, 2
	s_add_u32 s12, s4, s9
	s_addc_u32 s13, s5, 0
	global_load_dwordx4 v[16:19], v4, s[10:11]
	global_load_dwordx4 v[20:23], v4, s[10:11] offset:1024
	global_load_dwordx4 v[24:27], v4, s[10:11] offset:2048
	global_load_dwordx4 v[28:31], v4, s[10:11] offset:3072
	global_load_dwordx4 v[32:35], v5, s[10:11]
	global_load_dwordx4 v[36:39], v5, s[10:11] offset:1024
	global_load_dwordx4 v[40:43], v5, s[10:11] offset:2048
	global_load_dwordx4 v[44:47], v5, s[10:11] offset:3072
	global_load_dwordx4 v[48:51], v4, s[12:13]
	global_load_dwordx4 v[52:55], v4, s[12:13] offset:1024
	global_load_dwordx4 v[56:59], v4, s[12:13] offset:2048
	global_load_dwordx4 v[60:63], v4, s[12:13] offset:3072
	global_load_dwordx4 v[64:67], v5, s[12:13]
	global_load_dwordx4 v[68:71], v5, s[12:13] offset:1024
	global_load_dwordx4 v[72:75], v5, s[12:13] offset:2048
	global_load_dwordx4 v[76:79], v5, s[12:13] offset:3072
	v_mul_u32_u24_e32 v6, 0x840, v3
	v_lshl_add_u32 v6, v2, 4, v6
	v_add_u32_e32 v6, 0x4000, v6
	v_and_b32_e32 v8, 31, v0
	v_lshrrev_b32_e32 v9, 6, v0
	v_bfe_u32 v10, v0, 5, 1
	v_lshl_or_b32 v9, v9, 3, v10
	v_mul_u32_u24_e32 v7, 0x210, v8
	v_lshl_add_u32 v7, v9, 4, v7
	v_add_u32_e32 v7, 0x4000, v7
	s_waitcnt vmcnt(8)
	v_cvt_pk_f16_f32 v80, v16, v20
	v_cvt_pk_f16_f32 v81, v24, v28
	v_cvt_pk_f16_f32 v82, v32, v36
	v_cvt_pk_f16_f32 v83, v40, v44
	ds_write_b128 v6, v[80:83]
	v_cvt_pk_f16_f32 v84, v17, v21
	v_cvt_pk_f16_f32 v85, v25, v29
	v_cvt_pk_f16_f32 v86, v33, v37
	v_cvt_pk_f16_f32 v87, v41, v45
	ds_write_b128 v6, v[84:87] offset:528
	v_cvt_pk_f16_f32 v88, v18, v22
	v_cvt_pk_f16_f32 v89, v26, v30
	v_cvt_pk_f16_f32 v90, v34, v38
	v_cvt_pk_f16_f32 v91, v42, v46
	ds_write_b128 v6, v[88:91] offset:1056
	v_cvt_pk_f16_f32 v92, v19, v23
	v_cvt_pk_f16_f32 v93, v27, v31
	v_cvt_pk_f16_f32 v94, v35, v39
	v_cvt_pk_f16_f32 v95, v43, v47
	ds_write_b128 v6, v[92:95] offset:1584
	s_waitcnt vmcnt(0)
	v_cvt_pk_f16_f32 v80, v48, v52
	v_cvt_pk_f16_f32 v81, v56, v60
	v_cvt_pk_f16_f32 v82, v64, v68
	v_cvt_pk_f16_f32 v83, v72, v76
	ds_write_b128 v6, v[80:83] offset:16896
	v_cvt_pk_f16_f32 v84, v49, v53
	v_cvt_pk_f16_f32 v85, v57, v61
	v_cvt_pk_f16_f32 v86, v65, v69
	v_cvt_pk_f16_f32 v87, v73, v77
	ds_write_b128 v6, v[84:87] offset:17424
	v_cvt_pk_f16_f32 v88, v50, v54
	v_cvt_pk_f16_f32 v89, v58, v62
	v_cvt_pk_f16_f32 v90, v66, v70
	v_cvt_pk_f16_f32 v91, v74, v78
	ds_write_b128 v6, v[88:91] offset:17952
	v_cvt_pk_f16_f32 v92, v51, v55
	v_cvt_pk_f16_f32 v93, v59, v63
	v_cvt_pk_f16_f32 v94, v67, v71
	v_cvt_pk_f16_f32 v95, v75, v79
	ds_write_b128 v6, v[92:95] offset:18480
	s_waitcnt lgkmcnt(0)
	s_barrier
	ds_read_b128 v[16:19], v7
	ds_read_b128 v[32:35], v7 offset:16896
	ds_read_b128 v[20:23], v7 offset:32
	ds_read_b128 v[36:39], v7 offset:16928
	ds_read_b128 v[24:27], v7 offset:64
	ds_read_b128 v[40:43], v7 offset:16960
	ds_read_b128 v[28:31], v7 offset:96
	ds_read_b128 v[44:47], v7 offset:16992
	s_waitcnt lgkmcnt(6)
	v_mfma_f32_32x32x16_f16 a[0:15], v[16:19], v[32:35], 0
	s_waitcnt lgkmcnt(4)
	v_mfma_f32_32x32x16_f16 a[0:15], v[20:23], v[36:39], a[0:15]
	s_waitcnt lgkmcnt(2)
	v_mfma_f32_32x32x16_f16 a[0:15], v[24:27], v[40:43], a[0:15]
	s_waitcnt lgkmcnt(0)
	v_mfma_f32_32x32x16_f16 a[0:15], v[28:31], v[44:47], a[0:15]
	v_lshrrev_b32_e32 v2, 6, v0
	v_and_b32_e32 v3, 63, v0
	v_lshlrev_b32_e32 v2, 12, v2
	v_lshl_or_b32 v2, v3, 2, v2
	s_movk_i32 s4, 0x80
	v_cmp_gt_u32_e32 vcc, s4, v0
	s_nop 7
	ds_write_b32 v2, a0
	ds_write_b32 v2, a1 offset:256
	ds_write_b32 v2, a2 offset:512
	ds_write_b32 v2, a3 offset:768
	ds_write_b32 v2, a4 offset:1024
	ds_write_b32 v2, a5 offset:1280
	ds_write_b32 v2, a6 offset:1536
	ds_write_b32 v2, a7 offset:1792
	ds_write_b32 v2, a8 offset:2048
	ds_write_b32 v2, a9 offset:2304
	ds_write_b32 v2, a10 offset:2560
	ds_write_b32 v2, a11 offset:2816
	ds_write_b32 v2, a12 offset:3072
	ds_write_b32 v2, a13 offset:3328
	ds_write_b32 v2, a14 offset:3584
	ds_write_b32 v2, a15 offset:3840
	s_waitcnt lgkmcnt(0)
	s_barrier
	s_and_saveexec_b64 s[4:5], vcc
	s_cbranch_execz .LBB0_37
	v_lshrrev_b32_e32 v2, 3, v0
	v_and_b32_e32 v2, 12, v2
	v_and_b32_e32 v34, 3, v0
	v_and_or_b32 v2, v1, 3, v2
	v_lshlrev_b32_e32 v3, 3, v0
	v_and_b32_e32 v3, 0x80, v3
	v_lshlrev_b32_e32 v4, 5, v34
	v_lshlrev_b32_e32 v2, 8, v2
	v_or3_b32 v30, v3, v4, v2
	ds_read_b128 v[2:5], v30 offset:4096
	ds_read_b128 v[6:9], v30
	ds_read_b128 v[10:13], v30 offset:16
	ds_read_b128 v[14:17], v30 offset:8192
	ds_read_b128 v[18:21], v30 offset:12288
	ds_read_b128 v[22:25], v30 offset:4112
	s_waitcnt lgkmcnt(4)
	v_add_f32_e32 v2, v6, v2
	ds_read_b128 v[26:29], v30 offset:8208
	s_waitcnt lgkmcnt(3)
	v_add_f32_e32 v2, v2, v14
	s_waitcnt lgkmcnt(2)
	v_add_f32_e32 v2, v2, v18
	v_mul_f32_e32 v6, 0x43000000, v2
	v_add_f32_e32 v2, v7, v3
	v_add_f32_e32 v2, v2, v15
	v_add_f32_e32 v2, v2, v19
	v_mul_f32_e32 v7, 0x43000000, v2
	v_add_f32_e32 v2, v8, v4
	v_add_f32_e32 v2, v2, v16
	v_add_f32_e32 v2, v2, v20
	ds_read_b128 v[30:33], v30 offset:12304
	v_mul_f32_e32 v4, 0x43000000, v2
	v_add_f32_e32 v2, v9, v5
	v_add_f32_e32 v2, v2, v17
	v_add_f32_e32 v2, v2, v21
	v_mul_f32_e32 v5, 0x43000000, v2
	s_waitcnt lgkmcnt(2)
	v_add_f32_e32 v2, v10, v22
	s_waitcnt lgkmcnt(1)
	v_add_f32_e32 v2, v2, v26
	s_waitcnt lgkmcnt(0)
	v_add_f32_e32 v2, v2, v30
	v_mul_f32_e32 v8, 0x43000000, v2
	v_add_f32_e32 v2, v11, v23
	v_add_f32_e32 v2, v2, v27
	v_add_f32_e32 v2, v2, v31
	v_mul_f32_e32 v9, 0x43000000, v2
	v_add_f32_e32 v2, v12, v24
	v_add_f32_e32 v2, v2, v28
	v_add_f32_e32 v2, v2, v32
	v_mul_f32_e32 v10, 0x43000000, v2
	v_add_f32_e32 v2, v13, v25
	v_add_f32_e32 v11, v2, v29
	v_mov_b32_e32 v3, 0
	v_mov_b32_e32 v2, 0
	v_cvt_pk_fp8_f32 v2, v6, v7
	v_cvt_pk_fp8_f32 v3, v8, v9
	v_add_f32_e32 v6, v11, v33
	s_load_dwordx2 s[6:7], s[0:1], 0x38
	v_mul_f32_e32 v6, 0x43000000, v6
	v_cvt_pk_fp8_f32 v2, v4, v5 op_sel:[0,0,1]
	v_cvt_pk_fp8_f32 v3, v10, v6 op_sel:[0,0,1]
	s_lshl_b32 s3, s3, 8
	s_or_b32 s3, s3, s8
	v_lshlrev_b32_e32 v4, 3, v34
	v_or_b32_e32 v1, s3, v1
	v_lshl_or_b32 v1, v1, 5, v4
	s_waitcnt lgkmcnt(0)
	global_store_dwordx2 v1, v[2:3], s[6:7]

	.amdhsa_kernel _Z7na_prepPKfS0_S0_S0_S0_S0_PDF16_PhS1_PfS3_S3_
		.amdhsa_group_segment_fixed_size 50176
		.amdhsa_private_segment_fixed_size 0
		.amdhsa_kernarg_size 96
		.amdhsa_user_sgpr_count 2
		.amdhsa_user_sgpr_dispatch_ptr 0
		.amdhsa_user_sgpr_queue_ptr 0
		.amdhsa_user_sgpr_kernarg_segment_ptr 1
		.amdhsa_user_sgpr_dispatch_id 0
		.amdhsa_user_sgpr_kernarg_preload_length 0
		.amdhsa_user_sgpr_kernarg_preload_offset 0
		.amdhsa_user_sgpr_private_segment_size 0
		.amdhsa_uses_dynamic_stack 0
		.amdhsa_enable_private_segment 0
		.amdhsa_system_sgpr_workgroup_id_x 1
		.amdhsa_system_sgpr_workgroup_id_y 0
		.amdhsa_system_sgpr_workgroup_id_z 0
		.amdhsa_system_sgpr_workgroup_info 0
		.amdhsa_system_vgpr_workitem_id 0
		.amdhsa_next_free_vgpr 116
		.amdhsa_next_free_sgpr 17
		.amdhsa_accum_offset 100
		.amdhsa_reserve_vcc 1
		.amdhsa_float_round_mode_32 0
		.amdhsa_float_round_mode_16_64 0
		.amdhsa_float_denorm_mode_32 3
		.amdhsa_float_denorm_mode_16_64 3
		.amdhsa_dx10_clamp 1
		.amdhsa_ieee_mode 1
		.amdhsa_fp16_overflow 0
		.amdhsa_tg_split 0
		.amdhsa_exception_fp_ieee_invalid_op 0
		.amdhsa_exception_fp_denorm_src 0
		.amdhsa_exception_fp_ieee_div_zero 0
		.amdhsa_exception_fp_ieee_overflow 0
		.amdhsa_exception_fp_ieee_underflow 0
		.amdhsa_exception_fp_ieee_inexact 0
		.amdhsa_exception_int_div_zero 0
	.end_amdhsa_kernel

amdhsa.kernels:
  - .agpr_count:     16
    .args:
      - .actual_access:  read_only
        .address_space:  global
        .offset:         0
        .size:           8
        .value_kind:     global_buffer
      - .actual_access:  read_only
        .address_space:  global
        .offset:         8
        .size:           8
        .value_kind:     global_buffer
      - .actual_access:  read_only
        .address_space:  global
        .offset:         16
        .size:           8
        .value_kind:     global_buffer
      - .actual_access:  read_only
        .address_space:  global
        .offset:         24
        .size:           8
        .value_kind:     global_buffer
      - .actual_access:  read_only
        .address_space:  global
        .offset:         32
        .size:           8
        .value_kind:     global_buffer
      - .actual_access:  read_only
        .address_space:  global
        .offset:         40
        .size:           8
        .value_kind:     global_buffer
      - .actual_access:  write_only
        .address_space:  global
        .offset:         48
        .size:           8
        .value_kind:     global_buffer
      - .actual_access:  write_only
        .address_space:  global
        .offset:         56
        .size:           8
        .value_kind:     global_buffer
      - .actual_access:  write_only
        .address_space:  global
        .offset:         64
        .size:           8
        .value_kind:     global_buffer
      - .actual_access:  write_only
        .address_space:  global
        .offset:         72
        .size:           8
        .value_kind:     global_buffer
      - .actual_access:  write_only
        .address_space:  global
        .offset:         80
        .size:           8
        .value_kind:     global_buffer
      - .actual_access:  write_only
        .address_space:  global
        .offset:         88
        .size:           8
        .value_kind:     global_buffer
    .group_segment_fixed_size: 50176
    .kernarg_segment_align: 8
    .kernarg_segment_size: 96
    .language:       OpenCL C
    .language_version:
      - 2
      - 0
    .max_flat_workgroup_size: 256
    .name:           _Z7na_prepPKfS0_S0_S0_S0_S0_PDF16_PhS1_PfS3_S3_
    .private_segment_fixed_size: 0
    .sgpr_count:     23
    .sgpr_spill_count: 0
    .symbol:         _Z7na_prepPKfS0_S0_S0_S0_S0_PDF16_PhS1_PfS3_S3_.kd
    .uniform_work_group_size: 1
    .uses_dynamic_stack: false
    .vgpr_count:     116
    .vgpr_spill_count: 0
    .wavefront_size: 64
  - .agpr_count:     0
    .args:
      - .address_space:  global
        .offset:         0
        .size:           8
        .value_kind:     global_buffer
      - .actual_access:  read_only
        .address_space:  global
        .offset:         8
        .size:           8
        .value_kind:     global_buffer
      - .actual_access:  read_only
        .address_space:  global
        .offset:         16
        .size:           8
        .value_kind:     global_buffer
      - .actual_access:  read_only
        .address_space:  global
        .offset:         24
        .size:           8
        .value_kind:     global_buffer
      - .actual_access:  read_only
        .address_space:  global
        .offset:         32
        .size:           8
        .value_kind:     global_buffer
      - .actual_access:  read_only
        .address_space:  global
        .offset:         40
        .size:           8
        .value_kind:     global_buffer
      - .actual_access:  read_only
        .address_space:  global
        .offset:         48
        .size:           8
        .value_kind:     global_buffer
      - .actual_access:  write_only
        .address_space:  global
        .offset:         56
        .size:           8
        .value_kind:     global_buffer
    .group_segment_fixed_size: 162048
    .kernarg_segment_align: 8
    .kernarg_segment_size: 64
    .language:       OpenCL C
    .language_version:
      - 2
      - 0
    .max_flat_workgroup_size: 512
    .name:           _Z7na_mainPKDF16_PKhS0_PKfS4_S4_S4_Pf
    .private_segment_fixed_size: 0
    .sgpr_count:     24
    .sgpr_spill_count: 0
    .symbol:         _Z7na_mainPKDF16_PKhS0_PKfS4_S4_S4_Pf.kd
    .uniform_work_group_size: 1
    .uses_dynamic_stack: false
    .vgpr_count:     232
    .vgpr_spill_count: 0
    .wavefront_size: 64
